# stick-breaking step: computing waves issue the tile staging (LDS-DMA + scalar address work) behind their K-fragment LDS reads instead of at the step head
# speedup vs baseline: 1.0050x; 1.0050x over previous
; #define LAS __attribute__((address_space(3)))
; #define SB_STAGE(j_, so_) do { const size_t ro_ = (size_t)(j_) * 64 * D; glds16_s(Kwa + ro_, kvoff, kda + (so_)); glds16_s(Kwb + ro_, kvoff, kdb + (so_)); glds16_s(Vwa + ro_, vvoff, vda + (so_)); glds16_s(Vwb + ro_, vvoff, vdb + (so_)); } while (0)
; __device__ __forceinline__ void sb_block_unit(bf16x8 (&qr)[4], int b, int hp  , int u  , int nb, int nhp, int nu, const bf16_t* Q, const bf16_t* K, const bf16_t* V, bf16_t* O, LAS char* L, int wid, int lane) {
;     ...
;     f32x16 o[2]; o[0] = f32x16{}; o[1] = f32x16{};
;     float carry = 1.f; bool gone = false;
;     asm volatile("s_waitcnt vmcnt(0) lgkmcnt(0)\n\ts_barrier" ::: "memory");
;     int sc = 0, sn = SL_SLOT, sn2 = 2 * SL_SLOT;
;     for (int j = jtop; j >= 0; --j) {
;         if (j >= 2) SB_STAGE(j - 2, (unsigned)sn2);
;         if (j <= jdw && !gone) {
;             bf16x8 kf[8];
; #pragma unroll
;             for (int d0 = 0; d0 < 4; ++d0) { kf[2 * d0] = *(const LAS bf16x8*)(kp0 + sc + d0 * 2048); kf[2 * d0 + 1] = *(const LAS bf16x8*)(kp0 + sc + d0 * 2048 + 512); }
.LBB0_356:
	s_cmp_lt_u32 s33, 2
	s_cselect_b64 s[92:93], -1, 0
	s_mov_b32 s1, s88
	s_cmp_le_i32 s33, s97
	s_cselect_b64 s[100:101], -1, 0
	s_andn2_b64 s[100:101], s[100:101], s[4:5]
	s_and_b64 vcc, exec, s[92:93]
	s_cbranch_vccnz .LBB0_358
	s_cmp_lg_u64 s[100:101], 0
	s_cbranch_scc1 .LBB0_358
	v_readlane_b32 s86, v254, 55
	v_readlane_b32 s87, v254, 56
	s_mov_b32 s89, s87
	s_add_i32 s88, s33, -2
	v_writelane_b32 v254, s86, 55
	s_lshl_b64 s[88:89], s[88:89], 17
	s_add_u32 s94, s83, s88
	v_writelane_b32 v254, s87, 56
	s_addc_u32 s95, s80, s89
	v_readlane_b32 s86, v254, 5
	s_add_i32 s86, s84, s86
	s_mov_b32 s87, m0
	s_mov_b32 m0, s86
	s_nop 0
	global_load_lds_dwordx4 v142, s[94:95]
	s_mov_b32 m0, s87
	s_add_u32 s94, s3, s88
	v_readlane_b32 s86, v254, 7
	s_addc_u32 s95, s78, s89
	s_add_i32 s86, s84, s86
	s_mov_b32 s87, m0
	s_mov_b32 m0, s86
	s_nop 0
	global_load_lds_dwordx4 v142, s[94:95]
	s_mov_b32 m0, s87
	s_add_u32 s94, s2, s88
	v_readlane_b32 s86, v254, 9
	s_addc_u32 s95, s6, s89
	s_add_i32 s86, s84, s86
	s_mov_b32 s87, m0
	s_mov_b32 m0, s86
	s_nop 0
	global_load_lds_dwordx4 v145, s[94:95]
	s_mov_b32 m0, s87
	s_add_u32 s88, s81, s88
	v_readlane_b32 s86, v254, 11
	s_addc_u32 s89, s0, s89
	s_add_i32 s86, s84, s86
	s_mov_b32 s87, m0
	s_mov_b32 m0, s86
	s_nop 0
	global_load_lds_dwordx4 v145, s[88:89]
	s_mov_b32 m0, s87
.LBB0_358:
	s_cmp_le_i32 s33, s97
	s_cselect_b64 s[88:89], -1, 0
	s_xor_b64 s[94:95], s[4:5], -1
	s_and_b64 s[88:89], s[88:89], s[94:95]
	s_and_saveexec_b64 s[94:95], s[88:89]
	s_cbranch_execz .LBB0_370
	v_add_u32_e32 v38, s1, v146
	ds_read_b128 v[34:37], v38
	ds_read_b128 v[50:53], v38 offset:512
	ds_read_b128 v[82:85], v38 offset:2048
	ds_read_b128 v[86:89], v38 offset:2560
	ds_read_b128 v[90:93], v38 offset:4096
	ds_read_b128 v[94:97], v38 offset:4608
	ds_read_b128 v[98:101], v38 offset:6144
	ds_read_b128 v[102:105], v38 offset:6656
	s_cmp_lt_u32 s33, 2
	s_cbranch_scc1 .Lsbd_skip
	v_readlane_b32 s86, v254, 55
	v_readlane_b32 s87, v254, 56
	s_mov_b32 s89, s87
	s_add_i32 s88, s33, -2
	v_writelane_b32 v254, s86, 55
	s_lshl_b64 s[88:89], s[88:89], 17
	s_add_u32 s100, s83, s88
	v_writelane_b32 v254, s87, 56
	s_addc_u32 s101, s80, s89
	v_readlane_b32 s86, v254, 5
	s_add_i32 s86, s84, s86
	s_mov_b32 s87, m0
	s_mov_b32 m0, s86
	s_nop 0
	global_load_lds_dwordx4 v142, s[100:101]
	s_mov_b32 m0, s87
	s_add_u32 s100, s3, s88
	v_readlane_b32 s86, v254, 7
	s_addc_u32 s101, s78, s89
	s_add_i32 s86, s84, s86
	s_mov_b32 s87, m0
	s_mov_b32 m0, s86
	s_nop 0
	global_load_lds_dwordx4 v142, s[100:101]
	s_mov_b32 m0, s87
	s_add_u32 s100, s2, s88
	v_readlane_b32 s86, v254, 9
	s_addc_u32 s101, s6, s89
	s_add_i32 s86, s84, s86
	s_mov_b32 s87, m0
	s_mov_b32 m0, s86
	s_nop 0
	global_load_lds_dwordx4 v145, s[100:101]
	s_mov_b32 m0, s87
	s_add_u32 s88, s81, s88
	v_readlane_b32 s86, v254, 11
	s_addc_u32 s89, s0, s89
	s_add_i32 s86, s84, s86
	s_mov_b32 s87, m0
	s_mov_b32 m0, s86
	s_nop 0
	global_load_lds_dwordx4 v145, s[88:89]
	s_mov_b32 m0, s87
; #define LAS __attribute__((address_space(3)))
; __device__ __forceinline__ int crow(int r, int hi) { return (r & 3) + 8 * (r >> 2) + 4 * hi; }
; __device__ __forceinline__ s16x4 vtr(const LAS char* p) { return __builtin_bit_cast(s16x4, __builtin_amdgcn_ds_read_tr16_b64_v4i16((LAS v4i16_t*)p)); }
; __device__ __forceinline__ void pv_load(bf16x8 (&vf)[8], const LAS char* vp0) {
; #pragma unroll
;     for (int ks = 0; ks < 4; ++ks)
; #pragma unroll
;         for (int d0 = 0; d0 < 2; ++d0) {
;             const s16x4 lo = vtr(vp0 + d0 * 4096 + ks * 1024), hi4 = vtr(vp0 + d0 * 4096 + ks * 1024 + 512);
;             vf[2 * ks + d0] = (bf16x8){lo[0], lo[1], lo[2], lo[3], hi4[0], hi4[1], hi4[2], hi4[3]};
;         }
; }
; template <bool diag> __device__ __forceinline__ void sb_tile_math_t(f32x16& z0, f32x16& z1, float& carry, int s0, int tq, int hi) {
;         f32x16 q0, q1;
; #pragma unroll
;         for (int r = 0; r < 16; ++r) {
;             const int kv = s0 + crow(r, hi);
;             { float q = __builtin_amdgcn_rcpf(1.0f + __builtin_amdgcn_exp2f(z0[r])); if (diag && !(kv < tq)) q = 1.f; q0[r] = q; }
;             { float q = __builtin_amdgcn_rcpf(1.0f + __builtin_amdgcn_exp2f(z1[r])); if (diag && !(kv + 32 < tq)) q = 1.f; q1[r] = q; }
;         }
;         float own[8], oth[8], S[8];
; #pragma unroll
;         for (int G = 0; G < 4; ++G) { own[G] = (q0[4 * G] * q0[4 * G + 1]) * (q0[4 * G + 2] * q0[4 * G + 3]); own[4 + G] = (q1[4 * G] * q1[4 * G + 1]) * (q1[4 * G + 2] * q1[4 * G + 3]); }
; #pragma unroll
;         for (int i = 0; i < 8; ++i) { const auto rr = __builtin_amdgcn_permlane32_swap(__float_as_uint(own[i]), __float_as_uint(own[i]), false, false);
;             own[i] = __uint_as_float(rr[0]) * __uint_as_float(rr[1]); oth[i] = __uint_as_float(rr[1]); }
;         float run = 1.f;
; #pragma unroll
;         for (int i = 7; i >= 0; --i) { S[i] = run; run *= own[i]; }
.Lsbd_skip:
	s_waitcnt lgkmcnt(7)
	v_mfma_f32_32x32x16_bf16 v[34:49], v[34:37], v[66:69], 0
	s_waitcnt lgkmcnt(6)
	v_mfma_f32_32x32x16_bf16 v[50:65], v[50:53], v[66:69], 0
	s_waitcnt lgkmcnt(5)
	v_mfma_f32_32x32x16_bf16 v[34:49], v[82:85], v[70:73], v[34:49]
	s_waitcnt lgkmcnt(4)
	v_mfma_f32_32x32x16_bf16 v[50:65], v[86:89], v[70:73], v[50:65]
	s_waitcnt lgkmcnt(3)
	v_mfma_f32_32x32x16_bf16 v[34:49], v[90:93], v[74:77], v[34:49]
	v_add_u32_e32 v92, s1, v147
	s_waitcnt lgkmcnt(2)
	v_mfma_f32_32x32x16_bf16 v[50:65], v[94:97], v[74:77], v[50:65]
	s_waitcnt lgkmcnt(1)
	v_mfma_f32_32x32x16_bf16 v[34:49], v[98:101], v[78:81], v[34:49]
	s_waitcnt lgkmcnt(0)
	v_mfma_f32_32x32x16_bf16 v[50:65], v[102:105], v[78:81], v[50:65]
	ds_read_b64_tr_b16 v[110:111], v92 offset:8192
	ds_read_b64_tr_b16 v[112:113], v92 offset:8704
	ds_read_b64_tr_b16 v[106:107], v92 offset:12288
	ds_read_b64_tr_b16 v[108:109], v92 offset:12800
	ds_read_b64_tr_b16 v[102:103], v92 offset:9216
	ds_read_b64_tr_b16 v[104:105], v92 offset:9728
	ds_read_b64_tr_b16 v[98:99], v92 offset:13312
	ds_read_b64_tr_b16 v[100:101], v92 offset:13824
	ds_read_b64_tr_b16 v[94:95], v92 offset:10240
	ds_read_b64_tr_b16 v[96:97], v92 offset:10752
	ds_read_b64_tr_b16 v[86:87], v92 offset:14336
	ds_read_b64_tr_b16 v[88:89], v92 offset:14848
	ds_read_b64_tr_b16 v[82:83], v92 offset:11264
	ds_read_b64_tr_b16 v[84:85], v92 offset:11776
	ds_read_b64_tr_b16 v[90:91], v92 offset:15360
	ds_read_b64_tr_b16 v[92:93], v92 offset:15872
	v_exp_f32_e32 v34, v34
	v_exp_f32_e32 v179, v50
	v_exp_f32_e32 v177, v35
	v_exp_f32_e32 v175, v51
	v_add_f32_e32 v34, 1.0, v34
	v_rcp_f32_e32 v34, v34
	v_exp_f32_e32 v178, v36
	v_exp_f32_e32 v176, v52
	v_exp_f32_e32 v174, v37
	v_exp_f32_e32 v173, v53
	v_exp_f32_e32 v172, v38
	v_exp_f32_e32 v171, v54
	v_exp_f32_e32 v170, v39
	v_exp_f32_e32 v169, v55
	v_exp_f32_e32 v168, v40
	v_exp_f32_e32 v167, v56
	v_exp_f32_e32 v166, v41
	v_exp_f32_e32 v165, v57
	v_exp_f32_e32 v164, v42
	v_exp_f32_e32 v163, v58
	v_exp_f32_e32 v162, v43
	v_exp_f32_e32 v161, v59
	v_exp_f32_e32 v160, v44
	v_exp_f32_e32 v159, v60
	v_exp_f32_e32 v158, v45
	v_exp_f32_e32 v157, v61
	v_exp_f32_e32 v156, v46
	v_exp_f32_e32 v155, v62
	v_exp_f32_e32 v154, v47
	v_exp_f32_e32 v125, v63
	v_exp_f32_e32 v123, v48
	v_exp_f32_e32 v121, v64
	v_exp_f32_e32 v119, v49
	v_exp_f32_e32 v117, v65
	s_cmp_lg_u32 s96, s33
	s_mov_b64 vcc, -1
	s_cbranch_scc0 .LBB0_361
	v_add_f32_e32 v36, 1.0, v176
	v_rcp_f32_e32 v53, v36
	v_add_f32_e32 v36, 1.0, v174
	v_rcp_f32_e32 v47, v36
	v_add_f32_e32 v36, 1.0, v173
	v_rcp_f32_e32 v55, v36
	v_add_f32_e32 v36, 1.0, v172
	v_rcp_f32_e32 v56, v36
	v_add_f32_e32 v36, 1.0, v171
	v_rcp_f32_e32 v38, v36
	v_add_f32_e32 v36, 1.0, v170
	v_add_f32_e32 v35, 1.0, v179
	v_rcp_f32_e32 v58, v36
	v_add_f32_e32 v36, 1.0, v169
	v_rcp_f32_e32 v52, v35
	v_add_f32_e32 v35, 1.0, v177
	v_rcp_f32_e32 v44, v36
	v_add_f32_e32 v36, 1.0, v168
	v_rcp_f32_e32 v46, v35
	v_add_f32_e32 v35, 1.0, v175
	v_rcp_f32_e32 v57, v36
	v_add_f32_e32 v36, 1.0, v167
	v_rcp_f32_e32 v54, v35
	v_rcp_f32_e32 v39, v36
	v_add_f32_e32 v36, 1.0, v166
	v_add_f32_e32 v37, 1.0, v162
	v_rcp_f32_e32 v59, v36
	v_add_f32_e32 v36, 1.0, v165
	v_rcp_f32_e32 v64, v37
	v_add_f32_e32 v37, 1.0, v161
	v_rcp_f32_e32 v45, v36
	v_add_f32_e32 v36, 1.0, v164
	v_rcp_f32_e32 v42, v37
	v_add_f32_e32 v37, 1.0, v160
	v_add_f32_e32 v40, 1.0, v158
	v_add_f32_e32 v41, 1.0, v154
	v_rcp_f32_e32 v60, v36
	v_add_f32_e32 v36, 1.0, v163
	v_rcp_f32_e32 v61, v37
	v_add_f32_e32 v37, 1.0, v159
	v_rcp_f32_e32 v65, v40
	v_add_f32_e32 v40, 1.0, v157
	v_rcp_f32_e32 v132, v41
	v_add_f32_e32 v41, 1.0, v125
	v_rcp_f32_e32 v36, v36
	v_rcp_f32_e32 v37, v37
	v_rcp_f32_e32 v43, v40
	v_add_f32_e32 v40, 1.0, v156
	v_rcp_f32_e32 v48, v41
	v_add_f32_e32 v41, 1.0, v123
	v_add_f32_e32 v49, 1.0, v119
	v_pk_mul_f32 v[62:63], v[52:53], v[54:55]
	v_rcp_f32_e32 v128, v40
	v_rcp_f32_e32 v129, v41
	v_rcp_f32_e32 v133, v49
	v_pk_mul_f32 v[126:127], v[62:63], v[62:63] op_sel:[0,1] op_sel_hi:[1,0]
	v_pk_mul_f32 v[62:63], v[56:57], v[58:59]
	v_add_f32_e32 v35, 1.0, v178
	v_pk_mul_f32 v[130:131], v[62:63], v[62:63] op_sel:[0,1] op_sel_hi:[1,0]
	v_pk_mul_f32 v[62:63], v[38:39], v[44:45]
	v_add_f32_e32 v40, 1.0, v155
	v_pk_mul_f32 v[140:141], v[62:63], v[62:63] op_sel:[0,1] op_sel_hi:[1,0]
	v_pk_mul_f32 v[62:63], v[60:61], v[64:65]
	v_add_f32_e32 v41, 1.0, v121
	v_pk_mul_f32 v[134:135], v[62:63], v[62:63] op_sel:[0,1] op_sel_hi:[1,0]
	v_pk_mul_f32 v[62:63], v[36:37], v[42:43]
	v_add_f32_e32 v49, 1.0, v117
	v_pk_mul_f32 v[180:181], v[62:63], v[62:63] op_sel:[0,1] op_sel_hi:[1,0]
	v_pk_mul_f32 v[62:63], v[128:129], v[132:133]
	v_rcp_f32_e32 v35, v35
	v_rcp_f32_e32 v40, v40
	v_rcp_f32_e32 v41, v41
	v_rcp_f32_e32 v49, v49
	v_pk_mul_f32 v[138:139], v[62:63], v[62:63] op_sel:[0,1] op_sel_hi:[1,0]
	v_mov_b32_e32 v137, v134
	s_nop 1
	v_permlane32_swap_b32_e32 v134, v137
	v_mov_b32_e32 v135, v138
	v_mov_b32_e32 v131, v134
	s_nop 0
	v_permlane32_swap_b32_e32 v138, v135
	v_mov_b32_e32 v134, v126
	s_nop 1
	v_permlane32_swap_b32_e32 v126, v134
	v_mov_b32_e32 v127, v138
	v_pk_mul_f32 v[50:51], v[34:35], v[46:47]
	v_pk_mul_f32 v[62:63], v[40:41], v[48:49]
	v_pk_mul_f32 v[138:139], v[126:127], v[134:135]
	v_mov_b32_e32 v127, v140
	v_pk_mul_f32 v[50:51], v[50:51], v[50:51] op_sel:[0,1] op_sel_hi:[1,0]
	v_pk_mul_f32 v[62:63], v[62:63], v[62:63] op_sel:[0,1] op_sel_hi:[1,0]
	v_mov_b32_e32 v136, v130
	v_permlane32_swap_b32_e32 v140, v127
	v_mov_b32_e32 v126, v180
	v_mov_b32_e32 v63, v50
	v_permlane32_swap_b32_e32 v130, v136
	v_permlane32_swap_b32_e32 v180, v126
	v_mov_b32_e32 v181, v140
	v_mov_b32_e32 v51, v62
	v_permlane32_swap_b32_e32 v50, v63
	v_pk_mul_f32 v[130:131], v[130:131], v[136:137]
	v_pk_mul_f32 v[140:141], v[180:181], v[126:127]
	v_permlane32_swap_b32_e32 v62, v51
	s_mov_b64 vcc, 0
